# guard: conversion-at-barriers schedule only when the grid has 256 workgroups (otherwise the prologue converts everything as before)
# baseline (speedup 1.0000x reference)
.LBB0_133:
	s_add_i32 s46, s41, s33
	s_cmp_lg_u32 s92, 0x100
	s_cbranch_scc1 .Lp0_noskip
	s_add_i32 s2, s46, 0xfffff750
	s_cmp_lt_i32 s2, 0
	s_cbranch_scc1 .Lp0_noskip
	s_cmp_lt_i32 s2, 0x6000
	s_cbranch_scc1 .Lp0_skip
	s_add_i32 s2, s2, 0xffff9750
	s_cmp_lt_i32 s2, 0
	s_cbranch_scc1 .Lp0_noskip
	s_cmp_lt_i32 s2, 0x6000
	s_cbranch_scc1 .Lp0_skip
	s_add_i32 s2, s2, 0xffff9750
	s_cmp_lt_i32 s2, 0
	s_cbranch_scc1 .Lp0_noskip
	s_cmp_lt_i32 s2, 0x6000
	s_cbranch_scc1 .Lp0_skip
	s_add_i32 s2, s2, 0xffff9750
	s_cmp_lt_i32 s2, 0
	s_cbranch_scc1 .Lp0_noskip
	s_cmp_lt_i32 s2, 0x6000
	s_cbranch_scc1 .Lp0_skip
	s_branch .Lp0_noskip

.Lcvt_post:
	s_mov_b64 exec, -1
	s_waitcnt lgkmcnt(0)
	s_cmp_lg_u32 s92, 0x100
	s_cbranch_scc1 .Lcvt_ret
	v_lshrrev_b32_e32 v2, 6, v0
	v_and_b32_e32 v3, 63, v0
	s_nop 0
	v_readfirstlane_b32 s25, v2
	s_nop 3
	v_lshrrev_b32_e32 v4, 3, v3
	v_and_b32_e32 v5, 7, v3
	v_mul_u32_u24_e32 v7, 17, v4
	v_and_b32_e32 v8, 3, v3
	v_lshl_add_u32 v7, v8, 2, v7
	v_lshlrev_b32_e32 v7, 2, v7
	v_mul_u32_u24_e32 v8, 0x110, v5
	v_add_lshl_u32 v8, v8, v4, 2
	s_mul_i32 s17, s25, 0x2200
	v_add_u32_e32 v7, s17, v7
	v_add_u32_e32 v8, s17, v8
	v_lshlrev_b32_e32 v9, 10, v4
	v_lshl_add_u32 v9, v5, 4, v9
	v_add_u32_e32 v10, 0x2000, v9
	s_cmp_eq_u32 s31, 5
	s_cbranch_scc0 .Lcvt_t3
	s_cmp_ge_u32 s62, 3
	s_cbranch_scc1 .Lcvt_ret
	s_sub_i32 s27, s80, 16
	s_cmp_lt_i32 s27, 0
	s_cbranch_scc1 .Lcvt_ret
	s_mov_b32 s26, 3
	s_movk_i32 s30, 0
	s_movk_i32 s4, 5040
	s_mov_b32 s24, s62
	s_branch .Lcvt_go
